# baseline (speedup 1.0000x reference)
_ZN12_GLOBAL__N_113search_kernelEPKfS1_PhPf:
	s_load_dwordx2 s[8:9], s[0:1], 0x0
	s_load_dwordx2 s[4:5], s[0:1], 0x10
	s_movk_i32 s3, 0x90
	v_readfirstlane_b32 s10, v0
	v_cmp_gt_u32_e32 vcc, s3, v0
	s_and_saveexec_b64 s[6:7], vcc
	v_mov_b32_e32 v2, -1
	v_lshlrev_b32_e32 v1, 3, v0
	v_mov_b32_e32 v3, v2
	ds_write_b64 v1, v[2:3] offset:16384
	s_or_b64 exec, exec, s[6:7]
	s_waitcnt lgkmcnt(0)
	s_add_u32 s6, s4, 0x240000
	s_addc_u32 s7, s5, 0
	s_lshl_b32 s11, s2, 1
	s_and_b32 s14, s11, 14
	s_ashr_i32 s11, s2, 7
	s_lshr_b32 s15, s10, 6
	s_add_i32 s14, s14, s11
	s_bfe_u32 s2, s2, 0x40003
	s_mul_i32 s11, s15, 24
	v_mul_u32_u24_e32 v2, 0x71d, v0
	v_mul_u32_u24_e32 v4, 0x195, v0
	s_min_u32 s18, s11, 0xa5
	s_mul_i32 s11, s14, 3
	s_mul_i32 s12, s2, 9
	s_mov_b32 s13, 0
	v_lshrrev_b32_e32 v3, 16, v2
	s_movk_i32 s19, 0xffdc
	v_lshrrev_b32_e32 v5, 17, v4
	v_mad_i32_i24 v2, v3, s19, v0
	v_mad_i32_i24 v4, v5, -9, v3
	v_add_u32_e32 v3, s11, v5
	v_mov_b64_e32 v[6:7], s[12:13]
	v_mad_i64_i32 v[8:9], s[16:17], v3, s3, v[6:7]
	v_ashrrev_i32_e32 v5, 31, v4
	v_lshl_add_u64 v[4:5], v[8:9], 0, v[4:5]
	s_movk_i32 s13, 0x240
	v_mov_b64_e32 v[8:9], s[8:9]
	v_mad_u64_u32 v[10:11], s[8:9], v4, s13, v[8:9]
	v_min_u32_e32 v4, 0x1cb, v0
	v_or_b32_e32 v4, 0x200, v4
	v_mad_i32_i24 v11, v5, s13, v11
	v_mul_u32_u24_e32 v5, 0x71d, v4
	v_ashrrev_i32_e32 v3, 31, v2
	v_lshrrev_b32_e32 v5, 16, v5
	v_lshl_add_u64 v[2:3], v[2:3], 4, v[10:11]
	v_mad_i32_i24 v10, v5, s19, v4
	v_mul_u32_u24_e32 v4, 0x653, v4
	v_lshrrev_b32_e32 v11, 19, v4
	v_mad_i32_i24 v4, v11, -9, v5
	v_add_u32_e32 v5, s11, v11
	v_mad_i64_i32 v[6:7], s[8:9], v5, s3, v[6:7]
	v_ashrrev_i32_e32 v5, 31, v4
	v_lshl_add_u64 v[4:5], v[6:7], 0, v[4:5]
	v_mad_u64_u32 v[12:13], s[8:9], v4, s13, v[8:9]
	s_mul_i32 s8, s14, 0x90
	s_barrier
	s_load_dwordx2 s[42:43], s[0:1], 0x8
	v_mov_b32_e32 v16, 0
	v_mov_b32_e32 v17, 0
	ds_write_b64 v16, v[16:17] offset:18112
	global_load_dwordx4 v[6:9], v[2:3], off
	v_mad_i32_i24 v13, v5, s13, v13
	v_ashrrev_i32_e32 v11, 31, v10
	v_lshl_add_u64 v[10:11], v[10:11], 4, v[12:13]
	global_load_dwordx4 v[10:13], v[10:11], off
	v_and_b32_e32 v1, 63, v0
	s_add_i32 s20, s8, s12
	s_lshl_b32 s20, s20, 10
	v_lshl_add_u32 v164, v1, 4, s20
	s_mul_i32 s9, s14, 0xbd
	s_add_i32 s21, s9, s18
	s_lshl_b32 s21, s21, 10
	v_lshl_add_u32 v165, v1, 4, s21
	s_add_u32 s22, s4, 0x1000
	s_addc_u32 s23, s5, 0
	s_add_u32 s24, s4, 0x2000
	s_addc_u32 s25, s5, 0
	s_mov_b32 s26, s6
	s_mov_b32 s27, s7
	s_add_u32 s28, s6, 0x1000
	s_addc_u32 s29, s7, 0
	s_add_u32 s30, s6, 0x2000
	s_addc_u32 s31, s7, 0
	s_add_u32 s32, s6, 0x3000
	s_addc_u32 s33, s7, 0
	s_add_u32 s34, s6, 0x4000
	s_addc_u32 s35, s7, 0
	s_add_u32 s36, s6, 0x5000
	s_addc_u32 s37, s7, 0
	v_bfe_u32 v166, v0, 4, 2
	v_and_b32_e32 v167, 15, v0
	v_lshlrev_b32_e32 v167, 3, v167
	s_mul_i32 s40, s15, 6
	s_mov_b32 s41, 0x7f000000
	global_load_dwordx4 v[112:115], v164, s[4:5]
	global_load_dwordx4 v[16:19], v165, s[26:27] nt
	global_load_dwordx4 v[20:23], v165, s[26:27] offset:1024 nt
	global_load_dwordx4 v[24:27], v165, s[26:27] offset:2048 nt
	global_load_dwordx4 v[28:31], v165, s[26:27] offset:3072 nt
	global_load_dwordx4 v[32:35], v165, s[28:29] nt
	global_load_dwordx4 v[36:39], v165, s[28:29] offset:1024 nt
	global_load_dwordx4 v[40:43], v165, s[28:29] offset:2048 nt
	global_load_dwordx4 v[44:47], v165, s[28:29] offset:3072 nt
	global_load_dwordx4 v[48:51], v165, s[30:31] nt
	global_load_dwordx4 v[52:55], v165, s[30:31] offset:1024 nt
	global_load_dwordx4 v[56:59], v165, s[30:31] offset:2048 nt
	global_load_dwordx4 v[60:63], v165, s[30:31] offset:3072 nt
	global_load_dwordx4 v[64:67], v165, s[32:33] nt
	global_load_dwordx4 v[68:71], v165, s[32:33] offset:1024 nt
	global_load_dwordx4 v[72:75], v165, s[32:33] offset:2048 nt
	global_load_dwordx4 v[76:79], v165, s[32:33] offset:3072 nt
	global_load_dwordx4 v[80:83], v165, s[34:35] nt
	global_load_dwordx4 v[84:87], v165, s[34:35] offset:1024 nt
	global_load_dwordx4 v[88:91], v165, s[34:35] offset:2048 nt
	global_load_dwordx4 v[92:95], v165, s[34:35] offset:3072 nt
	global_load_dwordx4 v[96:99], v165, s[36:37] nt
	global_load_dwordx4 v[100:103], v165, s[36:37] offset:1024 nt
	global_load_dwordx4 v[104:107], v165, s[36:37] offset:2048 nt
	global_load_dwordx4 v[108:111], v165, s[36:37] offset:3072 nt
	global_load_dwordx4 v[116:119], v164, s[4:5] offset:1024
	v_lshlrev_b32_e32 v14, 4, v0
	s_lshr_b32 s50, s15, 1
	s_and_b32 s51, s15, 1
	s_lshl_b32 s51, s51, 3
	s_mov_b32 s48, 0x1010101
	s_mov_b32 s49, 0x1010101
	s_movk_i32 s58, 0x900
	s_movk_i32 s59, 0xb40
	v_and_b32_e32 v168, 7, v0
	v_lshrrev_b32_e32 v177, 3, v1
	v_or_b32_e32 v177, s51, v177
	v_lshlrev_b32_e32 v169, 3, v177
	v_and_b32_e32 v179, 3, v0
	v_lshlrev_b32_e32 v179, 8, v179
	v_lshl_add_u32 v170, v177, 4, v179
	v_add_u32_e32 v170, s20, v170
	v_lshrrev_b32_e32 v179, 2, v168
	v_and_b32_e32 v180, 3, v0
	v_lshl_or_b32 v171, v179, 4, v180
	v_mul_u32_u24_e32 v179, 11, v168
	v_lshrrev_b32_e32 v179, 5, v179
	v_mul_u32_u24_e32 v180, 3, v179
	v_sub_u32_e32 v180, v168, v180
	v_mul_u32_u24_e32 v181, 0x90, v179
	v_add_u32_e32 v181, v181, v180
	v_mul_u32_u24_e32 v172, 0x240, v181
	v_mul_u32_u24_e32 v181, 0x48, v179
	v_add_u32_e32 v181, v181, v180
	v_mul_u32_u24_e32 v173, 0x120, v181
	v_mul_u32_u24_e32 v181, 0x24, v179
	v_add_u32_e32 v181, v181, v180
	v_mul_u32_u24_e32 v174, 0x90, v181
	v_mul_u32_u24_e32 v181, 9, v179
	v_add_u32_e32 v181, v181, v180
	v_mul_u32_u24_e32 v175, 0x240, v181
	v_add_u32_e32 v176, 8, v168
	s_waitcnt lgkmcnt(0)
	s_mul_i32 s60, s14, 0x3cc00
	s_add_u32 s42, s42, s60
	s_addc_u32 s43, s43, 0
	s_mul_i32 s60, s14, 0xf300
	s_add_u32 s44, s4, s60
	s_addc_u32 s45, s5, 0
	s_add_u32 s44, s44, 0x534000
	s_addc_u32 s45, s45, 0
	s_mul_i32 s60, s14, 0x3cc0
	s_add_u32 s46, s4, s60
	s_addc_u32 s47, s5, 0
	s_add_u32 s46, s46, 0x627000
	s_addc_u32 s47, s47, 0
	v_mov_b32_e32 v152, s42
	v_mov_b32_e32 v153, s43
	v_mov_b32_e32 v154, s44
	v_mov_b32_e32 v155, s45
	v_mov_b32_e32 v159, s46
	v_mov_b32_e32 v161, s47
	s_load_dwordx2 s[2:3], s[0:1], 0x18
	s_waitcnt vmcnt(21)
	ds_write_b128 v14, v[6:9]
	ds_write_b128 v14, v[10:13] offset:8192
	v_mfma_f32_16x16x32_f16 v[120:123], v[16:19], v[112:115], 0
	v_mfma_f32_16x16x32_f16 v[124:127], v[20:23], v[112:115], 0
	v_mfma_f32_16x16x32_f16 v[128:131], v[24:27], v[112:115], 0
	v_mfma_f32_16x16x32_f16 v[132:135], v[28:31], v[112:115], 0
	s_waitcnt vmcnt(17)
	v_mfma_f32_16x16x32_f16 v[136:139], v[32:35], v[112:115], 0
	v_mfma_f32_16x16x32_f16 v[140:143], v[36:39], v[112:115], 0
	v_mfma_f32_16x16x32_f16 v[144:147], v[40:43], v[112:115], 0
	v_mfma_f32_16x16x32_f16 v[148:151], v[44:47], v[112:115], 0
	v_min3_i32 v160, v120, v121, s41
	v_min3_i32 v160, v122, v123, v160
	v_min3_i32 v160, v124, v125, v160
	v_min3_i32 v160, v126, v127, v160
	v_min3_i32 v160, v128, v129, v160
	v_min3_i32 v160, v130, v131, v160
	v_min3_i32 v160, v132, v133, v160
	v_min3_i32 v157, v134, v135, v160
	v_mov_b32_e32 v6, 0
	v_mov_b32_e32 v7, 0x900
	v_mov_b32_e32 v8, 0x240
	s_waitcnt vmcnt(13)
	v_mfma_f32_16x16x32_f16 v[120:123], v[48:51], v[112:115], 0
	v_mfma_f32_16x16x32_f16 v[124:127], v[52:55], v[112:115], 0
	v_mov_b32_e32 v158, 0
	v_mfma_f32_16x16x32_f16 v[128:131], v[56:59], v[112:115], 0
	v_mfma_f32_16x16x32_f16 v[132:135], v[60:63], v[112:115], 0
	v_min3_i32 v160, v136, v137, v157
	v_min3_i32 v160, v138, v139, v160
	v_min3_i32 v160, v140, v141, v160
	v_min3_i32 v160, v142, v143, v160
	v_min3_i32 v160, v144, v145, v160
	v_min3_i32 v160, v146, v147, v160
	v_min3_i32 v160, v148, v149, v160
	v_min3_i32 v156, v150, v151, v160
	v_cmp_ge_i32_e32 vcc, v156, v157
	s_waitcnt vmcnt(9)
	v_mfma_f32_16x16x32_f16 v[136:139], v[64:67], v[112:115], 0
	v_mfma_f32_16x16x32_f16 v[140:143], v[68:71], v[112:115], 0
	v_cndmask_b32_e32 v158, 1, v158, vcc
	v_mfma_f32_16x16x32_f16 v[144:147], v[72:75], v[112:115], 0
	v_mfma_f32_16x16x32_f16 v[148:151], v[76:79], v[112:115], 0
	v_min3_i32 v160, v120, v121, v156
	v_min3_i32 v160, v122, v123, v160
	v_min3_i32 v160, v124, v125, v160
	v_min3_i32 v160, v126, v127, v160
	v_min3_i32 v160, v128, v129, v160
	v_min3_i32 v160, v130, v131, v160
	v_min3_i32 v160, v132, v133, v160
	v_min3_i32 v157, v134, v135, v160
	v_cmp_ge_i32_e32 vcc, v157, v156
	s_waitcnt vmcnt(5)
	v_mfma_f32_16x16x32_f16 v[120:123], v[80:83], v[112:115], 0
	v_mfma_f32_16x16x32_f16 v[124:127], v[84:87], v[112:115], 0
	v_cndmask_b32_e32 v158, 2, v158, vcc
	v_mfma_f32_16x16x32_f16 v[128:131], v[88:91], v[112:115], 0
	v_mfma_f32_16x16x32_f16 v[132:135], v[92:95], v[112:115], 0
	v_min3_i32 v160, v136, v137, v157
	v_min3_i32 v160, v138, v139, v160
	v_min3_i32 v160, v140, v141, v160
	v_min3_i32 v160, v142, v143, v160
	v_min3_i32 v160, v144, v145, v160
	v_min3_i32 v160, v146, v147, v160
	v_min3_i32 v160, v148, v149, v160
	v_min3_i32 v156, v150, v151, v160
	v_cmp_ge_i32_e32 vcc, v156, v157
	s_waitcnt vmcnt(1)
	v_mfma_f32_16x16x32_f16 v[136:139], v[96:99], v[112:115], 0
	v_mfma_f32_16x16x32_f16 v[140:143], v[100:103], v[112:115], 0
	v_cndmask_b32_e32 v158, 3, v158, vcc
	v_mfma_f32_16x16x32_f16 v[144:147], v[104:107], v[112:115], 0
	v_mfma_f32_16x16x32_f16 v[148:151], v[108:111], v[112:115], 0
	v_min3_i32 v160, v120, v121, v156
	v_min3_i32 v160, v122, v123, v160
	v_min3_i32 v160, v124, v125, v160
	v_min3_i32 v160, v126, v127, v160
	v_min3_i32 v160, v128, v129, v160
	v_min3_i32 v160, v130, v131, v160
	v_min3_i32 v160, v132, v133, v160
	v_min3_i32 v157, v134, v135, v160
	v_cmp_ge_i32_e32 vcc, v157, v156
	s_waitcnt vmcnt(0)
	global_load_dwordx4 v[112:115], v164, s[4:5] offset:2048
	v_mfma_f32_16x16x32_f16 v[120:123], v[16:19], v[116:119], 0
	v_mfma_f32_16x16x32_f16 v[124:127], v[20:23], v[116:119], 0
	v_cndmask_b32_e32 v158, 4, v158, vcc
	v_mfma_f32_16x16x32_f16 v[128:131], v[24:27], v[116:119], 0
	v_mfma_f32_16x16x32_f16 v[132:135], v[28:31], v[116:119], 0
	v_min3_i32 v160, v136, v137, v157
	v_min3_i32 v160, v138, v139, v160
	v_min3_i32 v160, v140, v141, v160
	v_min3_i32 v160, v142, v143, v160
	v_min3_i32 v160, v144, v145, v160
	v_min3_i32 v160, v146, v147, v160
	v_min3_i32 v160, v148, v149, v160
	v_min3_i32 v156, v150, v151, v160
	v_cmp_ge_i32_e32 vcc, v156, v157
	v_mfma_f32_16x16x32_f16 v[136:139], v[32:35], v[116:119], 0
	v_mfma_f32_16x16x32_f16 v[140:143], v[36:39], v[116:119], 0
	v_cndmask_b32_e32 v158, 5, v158, vcc
	v_add_u32_e32 v162, s40, v158
	v_lshl_or_b32 v162, v162, 2, v166
	v_mov_b32_e32 v163, v156
	ds_min_u64 v167, v[162:163] offset:16384
	v_mfma_f32_16x16x32_f16 v[144:147], v[40:43], v[116:119], 0
	v_mfma_f32_16x16x32_f16 v[148:151], v[44:47], v[116:119], 0
	v_min3_i32 v160, v120, v121, s41
	v_min3_i32 v160, v122, v123, v160
	v_min3_i32 v160, v124, v125, v160
	v_min3_i32 v160, v126, v127, v160
	v_min3_i32 v160, v128, v129, v160
	v_min3_i32 v160, v130, v131, v160
	v_min3_i32 v160, v132, v133, v160
	v_min3_i32 v157, v134, v135, v160
	v_mfma_f32_16x16x32_f16 v[120:123], v[48:51], v[116:119], 0
	v_mfma_f32_16x16x32_f16 v[124:127], v[52:55], v[116:119], 0
	v_mov_b32_e32 v158, 0
	v_mfma_f32_16x16x32_f16 v[128:131], v[56:59], v[116:119], 0
	v_mfma_f32_16x16x32_f16 v[132:135], v[60:63], v[116:119], 0
	v_min3_i32 v160, v136, v137, v157
	v_min3_i32 v160, v138, v139, v160
	v_min3_i32 v160, v140, v141, v160
	v_min3_i32 v160, v142, v143, v160
	v_min3_i32 v160, v144, v145, v160
	v_min3_i32 v160, v146, v147, v160
	v_min3_i32 v160, v148, v149, v160
	v_min3_i32 v156, v150, v151, v160
	v_cmp_ge_i32_e32 vcc, v156, v157
	v_mfma_f32_16x16x32_f16 v[136:139], v[64:67], v[116:119], 0
	v_mfma_f32_16x16x32_f16 v[140:143], v[68:71], v[116:119], 0
	v_cndmask_b32_e32 v158, 1, v158, vcc
	v_mfma_f32_16x16x32_f16 v[144:147], v[72:75], v[116:119], 0
	v_mfma_f32_16x16x32_f16 v[148:151], v[76:79], v[116:119], 0
	v_min3_i32 v160, v120, v121, v156
	v_min3_i32 v160, v122, v123, v160
	v_min3_i32 v160, v124, v125, v160
	v_min3_i32 v160, v126, v127, v160
	v_min3_i32 v160, v128, v129, v160
	v_min3_i32 v160, v130, v131, v160
	v_min3_i32 v160, v132, v133, v160
	v_min3_i32 v157, v134, v135, v160
	v_cmp_ge_i32_e32 vcc, v157, v156
	v_mfma_f32_16x16x32_f16 v[120:123], v[80:83], v[116:119], 0
	v_mfma_f32_16x16x32_f16 v[124:127], v[84:87], v[116:119], 0
	v_cndmask_b32_e32 v158, 2, v158, vcc
	v_mfma_f32_16x16x32_f16 v[128:131], v[88:91], v[116:119], 0
	v_mfma_f32_16x16x32_f16 v[132:135], v[92:95], v[116:119], 0
	v_min3_i32 v160, v136, v137, v157
	v_min3_i32 v160, v138, v139, v160
	v_min3_i32 v160, v140, v141, v160
	v_min3_i32 v160, v142, v143, v160
	v_min3_i32 v160, v144, v145, v160
	v_min3_i32 v160, v146, v147, v160
	v_min3_i32 v160, v148, v149, v160
	v_min3_i32 v156, v150, v151, v160
	v_cmp_ge_i32_e32 vcc, v156, v157
	v_mfma_f32_16x16x32_f16 v[136:139], v[96:99], v[116:119], 0
	v_mfma_f32_16x16x32_f16 v[140:143], v[100:103], v[116:119], 0
	v_cndmask_b32_e32 v158, 3, v158, vcc
	v_mfma_f32_16x16x32_f16 v[144:147], v[104:107], v[116:119], 0
	v_mfma_f32_16x16x32_f16 v[148:151], v[108:111], v[116:119], 0
	v_min3_i32 v160, v120, v121, v156
	v_min3_i32 v160, v122, v123, v160
	v_min3_i32 v160, v124, v125, v160
	v_min3_i32 v160, v126, v127, v160
	v_min3_i32 v160, v128, v129, v160
	v_min3_i32 v160, v130, v131, v160
	v_min3_i32 v160, v132, v133, v160
	v_min3_i32 v157, v134, v135, v160
	v_cmp_ge_i32_e32 vcc, v157, v156
	s_waitcnt vmcnt(0)
	global_load_dwordx4 v[116:119], v164, s[4:5] offset:3072
	v_mfma_f32_16x16x32_f16 v[120:123], v[16:19], v[112:115], 0
	v_mfma_f32_16x16x32_f16 v[124:127], v[20:23], v[112:115], 0
	v_cndmask_b32_e32 v158, 4, v158, vcc
	v_mfma_f32_16x16x32_f16 v[128:131], v[24:27], v[112:115], 0
	v_mfma_f32_16x16x32_f16 v[132:135], v[28:31], v[112:115], 0
	v_min3_i32 v160, v136, v137, v157
	v_min3_i32 v160, v138, v139, v160
	v_min3_i32 v160, v140, v141, v160
	v_min3_i32 v160, v142, v143, v160
	v_min3_i32 v160, v144, v145, v160
	v_min3_i32 v160, v146, v147, v160
	v_min3_i32 v160, v148, v149, v160
	v_min3_i32 v156, v150, v151, v160
	v_cmp_ge_i32_e32 vcc, v156, v157
	v_mfma_f32_16x16x32_f16 v[136:139], v[32:35], v[112:115], 0
	v_mfma_f32_16x16x32_f16 v[140:143], v[36:39], v[112:115], 0
	v_cndmask_b32_e32 v158, 5, v158, vcc
	v_add_u32_e32 v162, s40, v158
	v_lshl_or_b32 v162, v162, 2, v166
	v_mov_b32_e32 v163, v156
	ds_min_u64 v167, v[162:163] offset:16512
	v_mfma_f32_16x16x32_f16 v[144:147], v[40:43], v[112:115], 0
	v_mfma_f32_16x16x32_f16 v[148:151], v[44:47], v[112:115], 0
	v_min3_i32 v160, v120, v121, s41
	v_min3_i32 v160, v122, v123, v160
	v_min3_i32 v160, v124, v125, v160
	v_min3_i32 v160, v126, v127, v160
	v_min3_i32 v160, v128, v129, v160
	v_min3_i32 v160, v130, v131, v160
	v_min3_i32 v160, v132, v133, v160
	v_min3_i32 v157, v134, v135, v160
	v_mfma_f32_16x16x32_f16 v[120:123], v[48:51], v[112:115], 0
	v_mfma_f32_16x16x32_f16 v[124:127], v[52:55], v[112:115], 0
	v_mov_b32_e32 v158, 0
	v_mfma_f32_16x16x32_f16 v[128:131], v[56:59], v[112:115], 0
	v_mfma_f32_16x16x32_f16 v[132:135], v[60:63], v[112:115], 0
	v_min3_i32 v160, v136, v137, v157
	v_min3_i32 v160, v138, v139, v160
	v_min3_i32 v160, v140, v141, v160
	v_min3_i32 v160, v142, v143, v160
	v_min3_i32 v160, v144, v145, v160
	v_min3_i32 v160, v146, v147, v160
	v_min3_i32 v160, v148, v149, v160
	v_min3_i32 v156, v150, v151, v160
	v_cmp_ge_i32_e32 vcc, v156, v157
	v_mfma_f32_16x16x32_f16 v[136:139], v[64:67], v[112:115], 0
	v_mfma_f32_16x16x32_f16 v[140:143], v[68:71], v[112:115], 0
	v_cndmask_b32_e32 v158, 1, v158, vcc
	v_mfma_f32_16x16x32_f16 v[144:147], v[72:75], v[112:115], 0
	v_mfma_f32_16x16x32_f16 v[148:151], v[76:79], v[112:115], 0
	v_min3_i32 v160, v120, v121, v156
	v_min3_i32 v160, v122, v123, v160
	v_min3_i32 v160, v124, v125, v160
	v_min3_i32 v160, v126, v127, v160
	v_min3_i32 v160, v128, v129, v160
	v_min3_i32 v160, v130, v131, v160
	v_min3_i32 v160, v132, v133, v160
	v_min3_i32 v157, v134, v135, v160
	v_cmp_ge_i32_e32 vcc, v157, v156
	v_mfma_f32_16x16x32_f16 v[120:123], v[80:83], v[112:115], 0
	v_mfma_f32_16x16x32_f16 v[124:127], v[84:87], v[112:115], 0
	v_cndmask_b32_e32 v158, 2, v158, vcc
	v_mfma_f32_16x16x32_f16 v[128:131], v[88:91], v[112:115], 0
	v_mfma_f32_16x16x32_f16 v[132:135], v[92:95], v[112:115], 0
	v_min3_i32 v160, v136, v137, v157
	v_min3_i32 v160, v138, v139, v160
	v_min3_i32 v160, v140, v141, v160
	v_min3_i32 v160, v142, v143, v160
	v_min3_i32 v160, v144, v145, v160
	v_min3_i32 v160, v146, v147, v160
	v_min3_i32 v160, v148, v149, v160
	v_min3_i32 v156, v150, v151, v160
	v_cmp_ge_i32_e32 vcc, v156, v157
	v_mfma_f32_16x16x32_f16 v[136:139], v[96:99], v[112:115], 0
	v_mfma_f32_16x16x32_f16 v[140:143], v[100:103], v[112:115], 0
	v_cndmask_b32_e32 v158, 3, v158, vcc
	v_mfma_f32_16x16x32_f16 v[144:147], v[104:107], v[112:115], 0
	v_mfma_f32_16x16x32_f16 v[148:151], v[108:111], v[112:115], 0
	v_min3_i32 v160, v120, v121, v156
	v_min3_i32 v160, v122, v123, v160
	v_min3_i32 v160, v124, v125, v160
	v_min3_i32 v160, v126, v127, v160
	v_min3_i32 v160, v128, v129, v160
	v_min3_i32 v160, v130, v131, v160
	v_min3_i32 v160, v132, v133, v160
	v_min3_i32 v157, v134, v135, v160
	v_cmp_ge_i32_e32 vcc, v157, v156
	s_waitcnt vmcnt(0)
	global_load_dwordx4 v[112:115], v164, s[22:23]
	v_mfma_f32_16x16x32_f16 v[120:123], v[16:19], v[116:119], 0
	v_mfma_f32_16x16x32_f16 v[124:127], v[20:23], v[116:119], 0
	v_cndmask_b32_e32 v158, 4, v158, vcc
	v_mfma_f32_16x16x32_f16 v[128:131], v[24:27], v[116:119], 0
	v_mfma_f32_16x16x32_f16 v[132:135], v[28:31], v[116:119], 0
	v_min3_i32 v160, v136, v137, v157
	v_min3_i32 v160, v138, v139, v160
	v_min3_i32 v160, v140, v141, v160
	v_min3_i32 v160, v142, v143, v160
	v_min3_i32 v160, v144, v145, v160
	v_min3_i32 v160, v146, v147, v160
	v_min3_i32 v160, v148, v149, v160
	v_min3_i32 v156, v150, v151, v160
	v_cmp_ge_i32_e32 vcc, v156, v157
	v_mfma_f32_16x16x32_f16 v[136:139], v[32:35], v[116:119], 0
	v_mfma_f32_16x16x32_f16 v[140:143], v[36:39], v[116:119], 0
	v_cndmask_b32_e32 v158, 5, v158, vcc
	v_add_u32_e32 v162, s40, v158
	v_lshl_or_b32 v162, v162, 2, v166
	v_mov_b32_e32 v163, v156
	ds_min_u64 v167, v[162:163] offset:16640
	v_mfma_f32_16x16x32_f16 v[144:147], v[40:43], v[116:119], 0
	v_mfma_f32_16x16x32_f16 v[148:151], v[44:47], v[116:119], 0
	v_min3_i32 v160, v120, v121, s41
	v_min3_i32 v160, v122, v123, v160
	v_min3_i32 v160, v124, v125, v160
	v_min3_i32 v160, v126, v127, v160
	v_min3_i32 v160, v128, v129, v160
	v_min3_i32 v160, v130, v131, v160
	v_min3_i32 v160, v132, v133, v160
	v_min3_i32 v157, v134, v135, v160
	v_mfma_f32_16x16x32_f16 v[120:123], v[48:51], v[116:119], 0
	v_mfma_f32_16x16x32_f16 v[124:127], v[52:55], v[116:119], 0
	v_mov_b32_e32 v158, 0
	v_mfma_f32_16x16x32_f16 v[128:131], v[56:59], v[116:119], 0
	v_mfma_f32_16x16x32_f16 v[132:135], v[60:63], v[116:119], 0
	v_min3_i32 v160, v136, v137, v157
	v_min3_i32 v160, v138, v139, v160
	v_min3_i32 v160, v140, v141, v160
	v_min3_i32 v160, v142, v143, v160
	v_min3_i32 v160, v144, v145, v160
	v_min3_i32 v160, v146, v147, v160
	v_min3_i32 v160, v148, v149, v160
	v_min3_i32 v156, v150, v151, v160
	v_cmp_ge_i32_e32 vcc, v156, v157
	v_mfma_f32_16x16x32_f16 v[136:139], v[64:67], v[116:119], 0
	v_mfma_f32_16x16x32_f16 v[140:143], v[68:71], v[116:119], 0
	v_cndmask_b32_e32 v158, 1, v158, vcc
	v_mfma_f32_16x16x32_f16 v[144:147], v[72:75], v[116:119], 0
	v_mfma_f32_16x16x32_f16 v[148:151], v[76:79], v[116:119], 0
	v_min3_i32 v160, v120, v121, v156
	v_min3_i32 v160, v122, v123, v160
	v_min3_i32 v160, v124, v125, v160
	v_min3_i32 v160, v126, v127, v160
	v_min3_i32 v160, v128, v129, v160
	v_min3_i32 v160, v130, v131, v160
	v_min3_i32 v160, v132, v133, v160
	v_min3_i32 v157, v134, v135, v160
	v_cmp_ge_i32_e32 vcc, v157, v156
	v_mfma_f32_16x16x32_f16 v[120:123], v[80:83], v[116:119], 0
	v_mfma_f32_16x16x32_f16 v[124:127], v[84:87], v[116:119], 0
	v_cndmask_b32_e32 v158, 2, v158, vcc
	v_mfma_f32_16x16x32_f16 v[128:131], v[88:91], v[116:119], 0
	v_mfma_f32_16x16x32_f16 v[132:135], v[92:95], v[116:119], 0
	v_min3_i32 v160, v136, v137, v157
	v_min3_i32 v160, v138, v139, v160
	v_min3_i32 v160, v140, v141, v160
	v_min3_i32 v160, v142, v143, v160
	v_min3_i32 v160, v144, v145, v160
	v_min3_i32 v160, v146, v147, v160
	v_min3_i32 v160, v148, v149, v160
	v_min3_i32 v156, v150, v151, v160
	v_cmp_ge_i32_e32 vcc, v156, v157
	v_mfma_f32_16x16x32_f16 v[136:139], v[96:99], v[116:119], 0
	v_mfma_f32_16x16x32_f16 v[140:143], v[100:103], v[116:119], 0
	v_cndmask_b32_e32 v158, 3, v158, vcc
	v_mfma_f32_16x16x32_f16 v[144:147], v[104:107], v[116:119], 0
	v_mfma_f32_16x16x32_f16 v[148:151], v[108:111], v[116:119], 0
	v_min3_i32 v160, v120, v121, v156
	v_min3_i32 v160, v122, v123, v160
	v_min3_i32 v160, v124, v125, v160
	v_min3_i32 v160, v126, v127, v160
	v_min3_i32 v160, v128, v129, v160
	v_min3_i32 v160, v130, v131, v160
	v_min3_i32 v160, v132, v133, v160
	v_min3_i32 v157, v134, v135, v160
	v_cmp_ge_i32_e32 vcc, v157, v156
	s_waitcnt vmcnt(0)
	global_load_dwordx4 v[116:119], v164, s[22:23] offset:1024
	v_mfma_f32_16x16x32_f16 v[120:123], v[16:19], v[112:115], 0
	v_mfma_f32_16x16x32_f16 v[124:127], v[20:23], v[112:115], 0
	v_cndmask_b32_e32 v158, 4, v158, vcc
	v_mfma_f32_16x16x32_f16 v[128:131], v[24:27], v[112:115], 0
	v_mfma_f32_16x16x32_f16 v[132:135], v[28:31], v[112:115], 0
	v_min3_i32 v160, v136, v137, v157
	v_min3_i32 v160, v138, v139, v160
	v_min3_i32 v160, v140, v141, v160
	v_min3_i32 v160, v142, v143, v160
	v_min3_i32 v160, v144, v145, v160
	v_min3_i32 v160, v146, v147, v160
	v_min3_i32 v160, v148, v149, v160
	v_min3_i32 v156, v150, v151, v160
	v_cmp_ge_i32_e32 vcc, v156, v157
	v_mfma_f32_16x16x32_f16 v[136:139], v[32:35], v[112:115], 0
	v_mfma_f32_16x16x32_f16 v[140:143], v[36:39], v[112:115], 0
	v_cndmask_b32_e32 v158, 5, v158, vcc
	v_add_u32_e32 v162, s40, v158
	v_lshl_or_b32 v162, v162, 2, v166
	v_mov_b32_e32 v163, v156
	ds_min_u64 v167, v[162:163] offset:16768
	v_mfma_f32_16x16x32_f16 v[144:147], v[40:43], v[112:115], 0
	v_mfma_f32_16x16x32_f16 v[148:151], v[44:47], v[112:115], 0
	v_min3_i32 v160, v120, v121, s41
	v_min3_i32 v160, v122, v123, v160
	v_min3_i32 v160, v124, v125, v160
	v_min3_i32 v160, v126, v127, v160
	v_min3_i32 v160, v128, v129, v160
	v_min3_i32 v160, v130, v131, v160
	v_min3_i32 v160, v132, v133, v160
	v_min3_i32 v157, v134, v135, v160
	v_mfma_f32_16x16x32_f16 v[120:123], v[48:51], v[112:115], 0
	v_mfma_f32_16x16x32_f16 v[124:127], v[52:55], v[112:115], 0
	v_mov_b32_e32 v158, 0
	v_mfma_f32_16x16x32_f16 v[128:131], v[56:59], v[112:115], 0
	v_mfma_f32_16x16x32_f16 v[132:135], v[60:63], v[112:115], 0
	v_min3_i32 v160, v136, v137, v157
	v_min3_i32 v160, v138, v139, v160
	v_min3_i32 v160, v140, v141, v160
	v_min3_i32 v160, v142, v143, v160
	v_min3_i32 v160, v144, v145, v160
	v_min3_i32 v160, v146, v147, v160
	v_min3_i32 v160, v148, v149, v160
	v_min3_i32 v156, v150, v151, v160
	v_cmp_ge_i32_e32 vcc, v156, v157
	v_mfma_f32_16x16x32_f16 v[136:139], v[64:67], v[112:115], 0
	v_mfma_f32_16x16x32_f16 v[140:143], v[68:71], v[112:115], 0
	v_cndmask_b32_e32 v158, 1, v158, vcc
	v_mfma_f32_16x16x32_f16 v[144:147], v[72:75], v[112:115], 0
	v_mfma_f32_16x16x32_f16 v[148:151], v[76:79], v[112:115], 0
	v_min3_i32 v160, v120, v121, v156
	v_min3_i32 v160, v122, v123, v160
	v_min3_i32 v160, v124, v125, v160
	v_min3_i32 v160, v126, v127, v160
	v_min3_i32 v160, v128, v129, v160
	v_min3_i32 v160, v130, v131, v160
	v_min3_i32 v160, v132, v133, v160
	v_min3_i32 v157, v134, v135, v160
	v_cmp_ge_i32_e32 vcc, v157, v156
	v_mfma_f32_16x16x32_f16 v[120:123], v[80:83], v[112:115], 0
	v_mfma_f32_16x16x32_f16 v[124:127], v[84:87], v[112:115], 0
	v_cndmask_b32_e32 v158, 2, v158, vcc
	v_mfma_f32_16x16x32_f16 v[128:131], v[88:91], v[112:115], 0
	v_mfma_f32_16x16x32_f16 v[132:135], v[92:95], v[112:115], 0
	v_min3_i32 v160, v136, v137, v157
	v_min3_i32 v160, v138, v139, v160
	v_min3_i32 v160, v140, v141, v160
	v_min3_i32 v160, v142, v143, v160
	v_min3_i32 v160, v144, v145, v160
	v_min3_i32 v160, v146, v147, v160
	v_min3_i32 v160, v148, v149, v160
	v_min3_i32 v156, v150, v151, v160
	v_cmp_ge_i32_e32 vcc, v156, v157
	v_mfma_f32_16x16x32_f16 v[136:139], v[96:99], v[112:115], 0
	v_mfma_f32_16x16x32_f16 v[140:143], v[100:103], v[112:115], 0
	v_cndmask_b32_e32 v158, 3, v158, vcc
	v_mfma_f32_16x16x32_f16 v[144:147], v[104:107], v[112:115], 0
	v_mfma_f32_16x16x32_f16 v[148:151], v[108:111], v[112:115], 0
	v_min3_i32 v160, v120, v121, v156
	v_min3_i32 v160, v122, v123, v160
	v_min3_i32 v160, v124, v125, v160
	v_min3_i32 v160, v126, v127, v160
	v_min3_i32 v160, v128, v129, v160
	v_min3_i32 v160, v130, v131, v160
	v_min3_i32 v160, v132, v133, v160
	v_min3_i32 v157, v134, v135, v160
	v_cmp_ge_i32_e32 vcc, v157, v156
	s_waitcnt vmcnt(0)
	global_load_dwordx4 v[112:115], v164, s[22:23] offset:2048
	v_mfma_f32_16x16x32_f16 v[120:123], v[16:19], v[116:119], 0
	v_mfma_f32_16x16x32_f16 v[124:127], v[20:23], v[116:119], 0
	v_cndmask_b32_e32 v158, 4, v158, vcc
	v_mfma_f32_16x16x32_f16 v[128:131], v[24:27], v[116:119], 0
	v_mfma_f32_16x16x32_f16 v[132:135], v[28:31], v[116:119], 0
	v_min3_i32 v160, v136, v137, v157
	v_min3_i32 v160, v138, v139, v160
	v_min3_i32 v160, v140, v141, v160
	v_min3_i32 v160, v142, v143, v160
	v_min3_i32 v160, v144, v145, v160
	v_min3_i32 v160, v146, v147, v160
	v_min3_i32 v160, v148, v149, v160
	v_min3_i32 v156, v150, v151, v160
	v_cmp_ge_i32_e32 vcc, v156, v157
	v_mfma_f32_16x16x32_f16 v[136:139], v[32:35], v[116:119], 0
	v_mfma_f32_16x16x32_f16 v[140:143], v[36:39], v[116:119], 0
	v_cndmask_b32_e32 v158, 5, v158, vcc
	v_add_u32_e32 v162, s40, v158
	v_lshl_or_b32 v162, v162, 2, v166
	v_mov_b32_e32 v163, v156
	ds_min_u64 v167, v[162:163] offset:16896
	v_mfma_f32_16x16x32_f16 v[144:147], v[40:43], v[116:119], 0
	v_mfma_f32_16x16x32_f16 v[148:151], v[44:47], v[116:119], 0
	v_min3_i32 v160, v120, v121, s41
	v_min3_i32 v160, v122, v123, v160
	v_min3_i32 v160, v124, v125, v160
	v_min3_i32 v160, v126, v127, v160
	v_min3_i32 v160, v128, v129, v160
	v_min3_i32 v160, v130, v131, v160
	v_min3_i32 v160, v132, v133, v160
	v_min3_i32 v157, v134, v135, v160
	v_mfma_f32_16x16x32_f16 v[120:123], v[48:51], v[116:119], 0
	v_mfma_f32_16x16x32_f16 v[124:127], v[52:55], v[116:119], 0
	v_mov_b32_e32 v158, 0
	v_mfma_f32_16x16x32_f16 v[128:131], v[56:59], v[116:119], 0
	v_mfma_f32_16x16x32_f16 v[132:135], v[60:63], v[116:119], 0
	v_min3_i32 v160, v136, v137, v157
	v_min3_i32 v160, v138, v139, v160
	v_min3_i32 v160, v140, v141, v160
	v_min3_i32 v160, v142, v143, v160
	v_min3_i32 v160, v144, v145, v160
	v_min3_i32 v160, v146, v147, v160
	v_min3_i32 v160, v148, v149, v160
	v_min3_i32 v156, v150, v151, v160
	v_cmp_ge_i32_e32 vcc, v156, v157
	v_mfma_f32_16x16x32_f16 v[136:139], v[64:67], v[116:119], 0
	v_mfma_f32_16x16x32_f16 v[140:143], v[68:71], v[116:119], 0
	v_cndmask_b32_e32 v158, 1, v158, vcc
	v_mfma_f32_16x16x32_f16 v[144:147], v[72:75], v[116:119], 0
	v_mfma_f32_16x16x32_f16 v[148:151], v[76:79], v[116:119], 0
	v_min3_i32 v160, v120, v121, v156
	v_min3_i32 v160, v122, v123, v160
	v_min3_i32 v160, v124, v125, v160
	v_min3_i32 v160, v126, v127, v160
	v_min3_i32 v160, v128, v129, v160
	v_min3_i32 v160, v130, v131, v160
	v_min3_i32 v160, v132, v133, v160
	v_min3_i32 v157, v134, v135, v160
	v_cmp_ge_i32_e32 vcc, v157, v156
	v_mfma_f32_16x16x32_f16 v[120:123], v[80:83], v[116:119], 0
	v_mfma_f32_16x16x32_f16 v[124:127], v[84:87], v[116:119], 0
	v_cndmask_b32_e32 v158, 2, v158, vcc
	v_mfma_f32_16x16x32_f16 v[128:131], v[88:91], v[116:119], 0
	v_mfma_f32_16x16x32_f16 v[132:135], v[92:95], v[116:119], 0
	v_min3_i32 v160, v136, v137, v157
	v_min3_i32 v160, v138, v139, v160
	v_min3_i32 v160, v140, v141, v160
	v_min3_i32 v160, v142, v143, v160
	v_min3_i32 v160, v144, v145, v160
	v_min3_i32 v160, v146, v147, v160
	v_min3_i32 v160, v148, v149, v160
	v_min3_i32 v156, v150, v151, v160
	v_cmp_ge_i32_e32 vcc, v156, v157
	v_mfma_f32_16x16x32_f16 v[136:139], v[96:99], v[116:119], 0
	v_mfma_f32_16x16x32_f16 v[140:143], v[100:103], v[116:119], 0
	v_cndmask_b32_e32 v158, 3, v158, vcc
	v_mfma_f32_16x16x32_f16 v[144:147], v[104:107], v[116:119], 0
	v_mfma_f32_16x16x32_f16 v[148:151], v[108:111], v[116:119], 0
	v_min3_i32 v160, v120, v121, v156
	v_min3_i32 v160, v122, v123, v160
	v_min3_i32 v160, v124, v125, v160
	v_min3_i32 v160, v126, v127, v160
	v_min3_i32 v160, v128, v129, v160
	v_min3_i32 v160, v130, v131, v160
	v_min3_i32 v160, v132, v133, v160
	v_min3_i32 v157, v134, v135, v160
	v_cmp_ge_i32_e32 vcc, v157, v156
	s_waitcnt vmcnt(0)
	global_load_dwordx4 v[116:119], v164, s[22:23] offset:3072
	v_mfma_f32_16x16x32_f16 v[120:123], v[16:19], v[112:115], 0
	v_mfma_f32_16x16x32_f16 v[124:127], v[20:23], v[112:115], 0
	v_cndmask_b32_e32 v158, 4, v158, vcc
	v_mfma_f32_16x16x32_f16 v[128:131], v[24:27], v[112:115], 0
	v_mfma_f32_16x16x32_f16 v[132:135], v[28:31], v[112:115], 0
	v_min3_i32 v160, v136, v137, v157
	v_min3_i32 v160, v138, v139, v160
	v_min3_i32 v160, v140, v141, v160
	v_min3_i32 v160, v142, v143, v160
	v_min3_i32 v160, v144, v145, v160
	v_min3_i32 v160, v146, v147, v160
	v_min3_i32 v160, v148, v149, v160
	v_min3_i32 v156, v150, v151, v160
	v_cmp_ge_i32_e32 vcc, v156, v157
	v_mfma_f32_16x16x32_f16 v[136:139], v[32:35], v[112:115], 0
	v_mfma_f32_16x16x32_f16 v[140:143], v[36:39], v[112:115], 0
	v_cndmask_b32_e32 v158, 5, v158, vcc
	v_add_u32_e32 v162, s40, v158
	v_lshl_or_b32 v162, v162, 2, v166
	v_mov_b32_e32 v163, v156
	ds_min_u64 v167, v[162:163] offset:17024
	v_mfma_f32_16x16x32_f16 v[144:147], v[40:43], v[112:115], 0
	v_mfma_f32_16x16x32_f16 v[148:151], v[44:47], v[112:115], 0
	v_min3_i32 v160, v120, v121, s41
	v_min3_i32 v160, v122, v123, v160
	v_min3_i32 v160, v124, v125, v160
	v_min3_i32 v160, v126, v127, v160
	v_min3_i32 v160, v128, v129, v160
	v_min3_i32 v160, v130, v131, v160
	v_min3_i32 v160, v132, v133, v160
	v_min3_i32 v157, v134, v135, v160
	s_waitcnt lgkmcnt(0)
	s_barrier
	s_lshl_b32 s60, s50, 7
	v_add_u32_e32 v2, s60, v169
	ds_read_b32 v178, v2 offset:16384
	s_lshl_b32 s60, s50, 10
	v_add_u32_e32 v210, s60, v170
	s_cmp_lt_u32 s50, 2
	s_cbranch_scc0 .Lp1a_y
	s_add_i32 s65, s50, 4
	s_lshl_b32 s60, s65, 7
	v_add_u32_e32 v2, s60, v169
	ds_read_b32 v216, v2 offset:16384
	s_lshl_b32 s60, s65, 10
	v_add_u32_e32 v248, s60, v170

	.amdhsa_kernel _ZN12_GLOBAL__N_113search_kernelEPKfS1_PhPf
		.amdhsa_group_segment_fixed_size 18144
		.amdhsa_private_segment_fixed_size 0
		.amdhsa_kernarg_size 32
		.amdhsa_user_sgpr_count 2
		.amdhsa_user_sgpr_dispatch_ptr 0
		.amdhsa_user_sgpr_queue_ptr 0
		.amdhsa_user_sgpr_kernarg_segment_ptr 1
		.amdhsa_user_sgpr_dispatch_id 0
		.amdhsa_user_sgpr_kernarg_preload_length 0
		.amdhsa_user_sgpr_kernarg_preload_offset 0
		.amdhsa_user_sgpr_private_segment_size 0
		.amdhsa_uses_dynamic_stack 0
		.amdhsa_enable_private_segment 0
		.amdhsa_system_sgpr_workgroup_id_x 1
		.amdhsa_system_sgpr_workgroup_id_y 0
		.amdhsa_system_sgpr_workgroup_id_z 0
		.amdhsa_system_sgpr_workgroup_info 0
		.amdhsa_system_vgpr_workitem_id 0
		.amdhsa_next_free_vgpr 256
		.amdhsa_next_free_sgpr 80
		.amdhsa_accum_offset 256
		.amdhsa_reserve_vcc 1
		.amdhsa_float_round_mode_32 0
		.amdhsa_float_round_mode_16_64 0
		.amdhsa_float_denorm_mode_32 3
		.amdhsa_float_denorm_mode_16_64 3
		.amdhsa_dx10_clamp 1
		.amdhsa_ieee_mode 1
		.amdhsa_fp16_overflow 0
		.amdhsa_tg_split 0
		.amdhsa_exception_fp_ieee_invalid_op 0
		.amdhsa_exception_fp_denorm_src 0
		.amdhsa_exception_fp_ieee_div_zero 0
		.amdhsa_exception_fp_ieee_overflow 0
		.amdhsa_exception_fp_ieee_underflow 0
		.amdhsa_exception_fp_ieee_inexact 0
		.amdhsa_exception_int_div_zero 0
	.end_amdhsa_kernel

amdhsa.kernels:
  - .agpr_count:     0
    .args:
      - .actual_access:  read_only
        .address_space:  global
        .offset:         0
        .size:           8
        .value_kind:     global_buffer
      - .actual_access:  read_only
        .address_space:  global
        .offset:         8
        .size:           8
        .value_kind:     global_buffer
      - .actual_access:  write_only
        .address_space:  global
        .offset:         16
        .size:           8
        .value_kind:     global_buffer
    .group_segment_fixed_size: 26112
    .kernarg_segment_align: 8
    .kernarg_segment_size: 24
    .language:       OpenCL C
    .language_version:
      - 2
      - 0
    .max_flat_workgroup_size: 256
    .name:           _ZN12_GLOBAL__N_111prep_kernelEPKfS1_Ph
    .private_segment_fixed_size: 0
    .sgpr_count:     25
    .sgpr_spill_count: 0
    .symbol:         _ZN12_GLOBAL__N_111prep_kernelEPKfS1_Ph.kd
    .uniform_work_group_size: 1
    .uses_dynamic_stack: false
    .vgpr_count:     34
    .vgpr_spill_count: 0
    .wavefront_size: 64
  - .agpr_count:     0
    .args:
      - .actual_access:  read_only
        .address_space:  global
        .offset:         0
        .size:           8
        .value_kind:     global_buffer
      - .actual_access:  read_only
        .address_space:  global
        .offset:         8
        .size:           8
        .value_kind:     global_buffer
      - .address_space:  global
        .offset:         16
        .size:           8
        .value_kind:     global_buffer
      - .actual_access:  write_only
        .address_space:  global
        .offset:         24
        .size:           8
        .value_kind:     global_buffer
    .group_segment_fixed_size: 18144
    .kernarg_segment_align: 8
    .kernarg_segment_size: 32
    .language:       OpenCL C
    .language_version:
      - 2
      - 0
    .max_flat_workgroup_size: 512
    .name:           _ZN12_GLOBAL__N_113search_kernelEPKfS1_PhPf
    .private_segment_fixed_size: 0
    .sgpr_count:     86
    .sgpr_spill_count: 0
    .symbol:         _ZN12_GLOBAL__N_113search_kernelEPKfS1_PhPf.kd
    .uniform_work_group_size: 1
    .uses_dynamic_stack: false
    .vgpr_count:     256
    .vgpr_spill_count: 0
    .wavefront_size: 64
